# speedup vs baseline: 1.0376x; 1.0335x over previous
.LBB1_51:
	s_or_b64 exec, exec, s[2:3]
	v_mad_i64_i32 v[22:23], s[2:3], v17, s56, 0
	v_mad_i64_i32 v[18:19], s[2:3], v18, s56, 0
	v_mad_i64_i32 v[24:25], s[2:3], v174, s56, 0
	v_readlane_b32 s3, v230, 8
	s_mov_b64 s[4:5], 0x80
	v_lshl_add_u64 v[6:7], v[6:7], 0, s[4:5]
	v_add_u32_e32 v128, s3, v16
	v_add_u32_e32 v129, 0x2000, v128
	v_readfirstlane_b32 s2, v128
	s_mov_b32 m0, s2
	v_readfirstlane_b32 s2, v129
	v_add_u32_e32 v130, 0x8000, v120
	v_mov_b32_e32 v66, 0
	v_mov_b32_e32 v67, 0
	v_mov_b32_e32 v68, 0
	v_mov_b32_e32 v69, 0
	v_mov_b32_e32 v78, 0
	v_mov_b32_e32 v79, 0
	v_mov_b32_e32 v80, 0
	v_mov_b32_e32 v81, 0
	v_mov_b32_e32 v82, 0
	v_mov_b32_e32 v83, 0
	v_mov_b32_e32 v84, 0
	v_mov_b32_e32 v85, 0
	v_mov_b32_e32 v86, 0
	v_mov_b32_e32 v87, 0
	v_mov_b32_e32 v88, 0
	v_mov_b32_e32 v89, 0
	v_mov_b32_e32 v90, 0
	v_mov_b32_e32 v91, 0
	v_mov_b32_e32 v92, 0
	v_mov_b32_e32 v93, 0
	v_mov_b32_e32 v94, 0
	v_mov_b32_e32 v95, 0
	v_mov_b32_e32 v96, 0
	v_mov_b32_e32 v97, 0
	v_mov_b32_e32 v26, 0
	v_mov_b32_e32 v27, 0
	v_mov_b32_e32 v28, 0
	v_mov_b32_e32 v29, 0
	v_mov_b32_e32 v30, 0
	v_mov_b32_e32 v31, 0
	v_mov_b32_e32 v32, 0
	v_mov_b32_e32 v33, 0
	v_mov_b32_e32 v34, 0
	v_mov_b32_e32 v35, 0
	v_mov_b32_e32 v36, 0
	v_mov_b32_e32 v37, 0
	v_mov_b32_e32 v38, 0
	v_mov_b32_e32 v39, 0
	v_mov_b32_e32 v40, 0
	v_mov_b32_e32 v41, 0
	v_mov_b32_e32 v46, 0
	v_mov_b32_e32 v47, 0
	v_mov_b32_e32 v48, 0
	v_mov_b32_e32 v49, 0
	v_mov_b32_e32 v54, 0
	v_mov_b32_e32 v55, 0
	v_mov_b32_e32 v56, 0
	v_mov_b32_e32 v57, 0
	v_mov_b32_e32 v42, 0
	v_mov_b32_e32 v43, 0
	v_mov_b32_e32 v44, 0
	v_mov_b32_e32 v45, 0
	v_mov_b32_e32 v50, 0
	v_mov_b32_e32 v51, 0
	v_mov_b32_e32 v52, 0
	v_mov_b32_e32 v53, 0
	v_mov_b32_e32 v58, 0
	v_mov_b32_e32 v59, 0
	v_mov_b32_e32 v60, 0
	v_mov_b32_e32 v61, 0
	v_mov_b32_e32 v62, 0
	v_mov_b32_e32 v63, 0
	v_mov_b32_e32 v64, 0
	v_mov_b32_e32 v65, 0
	v_mov_b32_e32 v70, 0
	v_mov_b32_e32 v71, 0
	v_mov_b32_e32 v72, 0
	v_mov_b32_e32 v73, 0
	v_mov_b32_e32 v74, 0
	v_mov_b32_e32 v75, 0
	v_mov_b32_e32 v76, 0
	v_mov_b32_e32 v77, 0
	s_waitcnt vmcnt(4)
	s_barrier
	global_load_lds_dwordx4 v[6:7], off
	v_lshl_add_u64 v[6:7], v[8:9], 0, s[4:5]
	s_mov_b32 m0, s2
	v_readfirstlane_b32 s2, v130
	v_add_u32_e32 v131, 0xa000, v120
	global_load_lds_dwordx4 v[6:7], off
	v_lshl_add_u64 v[6:7], v[10:11], 0, s[4:5]
	s_mov_b32 m0, s2
	v_readfirstlane_b32 s2, v131
	global_load_lds_dwordx4 v[6:7], off
	v_lshl_add_u64 v[6:7], v[12:13], 0, s[4:5]
	s_mov_b32 m0, s2
	s_mov_b64 s[4:5], 0x24080
	global_load_lds_dwordx4 v[6:7], off
	v_lshl_add_u64 v[6:7], v[14:15], 0, s[4:5]
	v_readlane_b32 s4, v230, 9
	v_lshl_add_u64 v[8:9], v[6:7], 0, v[22:23]
	v_lshl_add_u64 v[8:9], v[8:9], 0, v[2:3]
	v_add_u32_e32 v132, s4, v16
	v_add_u32_e32 v133, 0x2000, v132
	v_readfirstlane_b32 s2, v132
	s_mov_b32 m0, s2
	v_lshl_add_u64 v[6:7], v[6:7], 0, v[18:19]
	v_readfirstlane_b32 s2, v133
	global_load_lds_dwordx4 v[8:9], off
	v_lshl_add_u64 v[6:7], v[6:7], 0, v[4:5]
	s_mov_b32 m0, s2
	v_and_b32_e32 v177, 15, v175
	global_load_lds_dwordx4 v[6:7], off
	v_and_b32_e32 v6, 64, v175
	v_lshlrev_b32_e32 v8, 2, v175
	v_cmp_ne_u32_e32 vcc, 0, v6
	v_and_b32_e32 v6, 48, v175
	v_lshlrev_b32_e32 v7, 6, v177
	v_and_b32_e32 v8, 32, v8
	v_bitop3_b32 v7, v7, v8, v6 bitop3:0x36
	v_readlane_b32 s2, v230, 6
	v_ashrrev_i32_e32 v10, 2, v175
	v_and_b32_e32 v180, 0xffffffe0, v10
	v_add_u32_e32 v9, s2, v7
	v_readlane_b32 s2, v230, 7
	v_add_u32_e32 v11, s3, v7
	v_add_u32_e32 v12, s4, v7
	v_add_u32_e32 v10, s2, v7
	v_add_u32_e32 v14, 0, v7
	v_lshlrev_b32_e32 v7, 6, v175
	s_movk_i32 s2, 0x3c0
	v_mul_u32_u24_e32 v20, 0x600, v118
	v_mov_b32_e32 v21, v109
	v_and_or_b32 v6, v7, s2, v6
	v_lshl_add_u64 v[2:3], v[22:23], 0, v[2:3]
	v_xad_u32 v8, v6, v8, 0
	v_lshl_add_u64 v[6:7], v[2:3], 0, v[20:21]
	v_lshl_add_u64 v[4:5], v[18:19], 0, v[4:5]
	v_lshl_add_u64 v[102:103], s[42:43], 0, v[6:7]
	v_lshl_add_u64 v[6:7], v[4:5], 0, v[20:21]
	v_lshl_add_u64 v[104:105], s[42:43], 0, v[6:7]
	v_lshl_add_u64 v[6:7], v[2:3], 0, v[24:25]
	v_lshl_add_u64 v[2:3], v[2:3], 0, v[108:109]
	v_cndmask_b32_e64 v179, 0, 48, vcc
	v_lshlrev_b32_e32 v15, 7, v180
	v_lshl_add_u64 v[114:115], s[42:43], 0, v[2:3]
	v_lshl_add_u64 v[2:3], v[4:5], 0, v[108:109]
	v_lshlrev_b32_e32 v13, 7, v179
	v_or_b32_e32 v16, 0x800, v15
	v_lshl_add_u64 v[110:111], s[44:45], 0, v[6:7]
	v_lshl_add_u64 v[6:7], v[4:5], 0, v[24:25]
	v_lshl_add_u64 v[116:117], s[42:43], 0, v[2:3]
	v_mov_b32_e32 v2, 0
	v_lshl_add_u64 v[112:113], s[44:45], 0, v[6:7]
	s_mov_b32 s4, -2
	s_mov_b64 s[2:3], 0
	v_add_u32_e32 v135, v9, v13
	v_add_u32_e32 v121, v14, v15
	v_add_u32_e32 v108, v8, v16
	v_add_u32_e32 v134, v10, v13
	v_add_u32_e32 v127, v11, v13
	v_add_u32_e32 v124, v12, v13
	v_mov_b32_e32 v3, v2
	v_mov_b32_e32 v4, v2
	v_mov_b32_e32 v5, v2
	v_mov_b32_e32 v6, v2
	v_mov_b32_e32 v7, v2
	v_mov_b32_e32 v8, v2
	v_mov_b32_e32 v9, v2
	v_mov_b32_e32 v10, v2
	v_mov_b32_e32 v11, v2
	v_mov_b32_e32 v12, v2
	v_mov_b32_e32 v13, v2
	v_mov_b32_e32 v14, v2
	v_mov_b32_e32 v15, v2
	v_mov_b32_e32 v16, v2
	v_mov_b32_e32 v17, v2
	v_mov_b32_e32 v18, v2
	v_mov_b32_e32 v19, v2
	v_mov_b32_e32 v20, v2
	v_mov_b32_e32 v21, v2
	v_mov_b32_e32 v22, v2
	v_mov_b32_e32 v23, v2
	v_mov_b32_e32 v24, v2
	v_mov_b32_e32 v25, v2
	s_waitcnt vmcnt(6)
	s_barrier
	v_add_u32_e32 v136, 0xc000, v120
	v_add_u32_e32 v137, 0xe000, v120
	v_readfirstlane_b32 s12, v120
	v_subrev_u32_e32 v248, s44, v110
	v_subrev_u32_e32 v249, s44, v112
	v_subrev_u32_e32 v250, s42, v102
	v_subrev_u32_e32 v251, s42, v104
	v_subrev_u32_e32 v246, s42, v114
	v_subrev_u32_e32 v247, s42, v116
	v_add_u32_e32 v232, 0x100, v248
	v_add_u32_e32 v233, 0x100, v249
	v_add_u32_e32 v234, 0x180, v248
	v_add_u32_e32 v235, 0x180, v249
	v_add_u32_e32 v236, 0x30080, v248
	v_add_u32_e32 v237, 0x30080, v249
	v_add_u32_e32 v238, 0x30100, v248
	v_add_u32_e32 v239, 0x30100, v249
	v_add_u32_e32 v240, 0x100, v250
	v_add_u32_e32 v241, 0x100, v251
	v_add_u32_e32 v242, 0x180, v250
	v_add_u32_e32 v243, 0x180, v251
	v_add_u32_e32 v244, 0x24100, v246
	v_add_u32_e32 v245, 0x24100, v247
	v_add_u32_e32 v246, 0x24180, v246
	v_add_u32_e32 v247, 0x24180, v247
	s_add_u32 s8, s44, s2
	s_addc_u32 s9, s45, s3
	s_add_u32 s10, s42, s2
	s_addc_u32 s11, s43, s3
.LBB1_52:
	ds_read_b128 v[138:141], v135
	ds_read_b128 v[142:145], v135 offset:1024
	ds_read_b128 v[146:149], v135 offset:2048
	ds_read_b128 v[150:153], v135 offset:3072
	ds_read_b128 v[154:157], v135 offset:4096
	ds_read_b128 v[158:161], v135 offset:5120
	s_add_u32 m0, s12, 0xc000
	ds_read_b128 v[162:165], v121
	ds_read_b128 v[182:185], v121 offset:1024
	ds_read_b128 v[186:189], v108
	ds_read_b128 v[190:193], v108 offset:1024
	global_load_lds_dwordx4 v236, s[8:9]
	s_add_u32 m0, s12, 0xe000
	s_nop 0
	global_load_lds_dwordx4 v237, s[8:9]
	s_waitcnt lgkmcnt(4)
	s_barrier
	s_waitcnt lgkmcnt(0)
	s_setprio 1
	s_waitcnt lgkmcnt(0)
	v_mfma_f32_16x16x32_f16 v[94:97], v[162:165], v[138:141], v[94:97]
	v_mfma_f32_16x16x32_f16 v[90:93], v[162:165], v[146:149], v[90:93]
	v_mfma_f32_16x16x32_f16 v[86:89], v[162:165], v[154:157], v[86:89]
	v_mfma_f32_16x16x32_f16 v[82:85], v[186:189], v[138:141], v[82:85]
	v_mfma_f32_16x16x32_f16 v[78:81], v[186:189], v[146:149], v[78:81]
	v_mfma_f32_16x16x32_f16 v[66:69], v[186:189], v[154:157], v[66:69]
	v_mfma_f32_16x16x32_f16 v[94:97], v[182:185], v[142:145], v[94:97]
	v_mfma_f32_16x16x32_f16 v[90:93], v[182:185], v[150:153], v[90:93]
	v_mfma_f32_16x16x32_f16 v[86:89], v[182:185], v[158:161], v[86:89]
	v_mfma_f32_16x16x32_f16 v[82:85], v[190:193], v[142:145], v[82:85]
	v_mfma_f32_16x16x32_f16 v[78:81], v[190:193], v[150:153], v[78:81]
	v_mfma_f32_16x16x32_f16 v[66:69], v[190:193], v[158:161], v[66:69]
	s_setprio 0
	s_barrier
	s_add_u32 m0, s12, 0x10000
	ds_read_b128 v[194:197], v134
	ds_read_b128 v[198:201], v134 offset:1024
	ds_read_b128 v[202:205], v134 offset:2048
	ds_read_b128 v[206:209], v134 offset:3072
	ds_read_b128 v[210:213], v134 offset:4096
	ds_read_b128 v[214:217], v134 offset:5120
	global_load_lds_dwordx4 v240, s[10:11]
	s_add_u32 m0, s12, 0x12000
	s_nop 0
	global_load_lds_dwordx4 v241, s[10:11]
	s_barrier
	s_waitcnt lgkmcnt(0)
	s_setprio 1
	s_waitcnt lgkmcnt(0)
	v_mfma_f32_16x16x32_f16 v[22:25], v[162:165], v[194:197], v[22:25]
	v_mfma_f32_16x16x32_f16 v[18:21], v[162:165], v[202:205], v[18:21]
	v_mfma_f32_16x16x32_f16 v[14:17], v[162:165], v[210:213], v[14:17]
	v_mfma_f32_16x16x32_f16 v[10:13], v[186:189], v[194:197], v[10:13]
	v_mfma_f32_16x16x32_f16 v[6:9], v[186:189], v[202:205], v[6:9]
	v_mfma_f32_16x16x32_f16 v[2:5], v[186:189], v[210:213], v[2:5]
	v_mfma_f32_16x16x32_f16 v[22:25], v[182:185], v[198:201], v[22:25]
	v_mfma_f32_16x16x32_f16 v[18:21], v[182:185], v[206:209], v[18:21]
	v_mfma_f32_16x16x32_f16 v[14:17], v[182:185], v[214:217], v[14:17]
	v_mfma_f32_16x16x32_f16 v[10:13], v[190:193], v[198:201], v[10:13]
	v_mfma_f32_16x16x32_f16 v[6:9], v[190:193], v[206:209], v[6:9]
	v_mfma_f32_16x16x32_f16 v[2:5], v[190:193], v[214:217], v[2:5]
	s_setprio 0
	s_add_u32 m0, s12, 0x0
	s_barrier
	ds_read_b128 v[162:165], v121 offset:16384
	ds_read_b128 v[182:185], v121 offset:17408
	ds_read_b128 v[186:189], v108 offset:16384
	ds_read_b128 v[190:193], v108 offset:17408
	global_load_lds_dwordx4 v232, s[8:9]
	s_add_u32 m0, s12, 0x2000
	s_nop 0
	global_load_lds_dwordx4 v233, s[8:9]
	s_barrier
	s_waitcnt lgkmcnt(0)
	s_setprio 1
	s_waitcnt lgkmcnt(0)
	v_mfma_f32_16x16x32_f16 v[26:29], v[162:165], v[138:141], v[26:29]
	v_mfma_f32_16x16x32_f16 v[30:33], v[162:165], v[146:149], v[30:33]
	v_mfma_f32_16x16x32_f16 v[34:37], v[162:165], v[154:157], v[34:37]
	v_mfma_f32_16x16x32_f16 v[38:41], v[186:189], v[138:141], v[38:41]
	v_mfma_f32_16x16x32_f16 v[46:49], v[186:189], v[146:149], v[46:49]
	v_mfma_f32_16x16x32_f16 v[54:57], v[186:189], v[154:157], v[54:57]
	v_mfma_f32_16x16x32_f16 v[26:29], v[182:185], v[142:145], v[26:29]
	v_mfma_f32_16x16x32_f16 v[30:33], v[182:185], v[150:153], v[30:33]
	v_mfma_f32_16x16x32_f16 v[34:37], v[182:185], v[158:161], v[34:37]
	v_mfma_f32_16x16x32_f16 v[38:41], v[190:193], v[142:145], v[38:41]
	v_mfma_f32_16x16x32_f16 v[46:49], v[190:193], v[150:153], v[46:49]
	v_mfma_f32_16x16x32_f16 v[54:57], v[190:193], v[158:161], v[54:57]
	s_setprio 0
	s_barrier
	s_add_u32 m0, s12, 0x14000
	s_nop 0
	global_load_lds_dwordx4 v244, s[10:11]
	s_add_u32 m0, s12, 0x16000
	s_nop 0
	global_load_lds_dwordx4 v245, s[10:11]
	s_waitcnt vmcnt(6)
	s_barrier
	s_setprio 1
	v_mfma_f32_16x16x32_f16 v[42:45], v[162:165], v[194:197], v[42:45]
	v_mfma_f32_16x16x32_f16 v[50:53], v[162:165], v[202:205], v[50:53]
	v_mfma_f32_16x16x32_f16 v[58:61], v[162:165], v[210:213], v[58:61]
	v_mfma_f32_16x16x32_f16 v[62:65], v[186:189], v[194:197], v[62:65]
	v_mfma_f32_16x16x32_f16 v[70:73], v[186:189], v[202:205], v[70:73]
	v_mfma_f32_16x16x32_f16 v[74:77], v[186:189], v[210:213], v[74:77]
	v_mfma_f32_16x16x32_f16 v[42:45], v[182:185], v[198:201], v[42:45]
	v_mfma_f32_16x16x32_f16 v[50:53], v[182:185], v[206:209], v[50:53]
	v_mfma_f32_16x16x32_f16 v[58:61], v[182:185], v[214:217], v[58:61]
	v_mfma_f32_16x16x32_f16 v[62:65], v[190:193], v[198:201], v[62:65]
	v_mfma_f32_16x16x32_f16 v[70:73], v[190:193], v[206:209], v[70:73]
	v_mfma_f32_16x16x32_f16 v[74:77], v[190:193], v[214:217], v[74:77]
	s_setprio 0
	s_barrier
	ds_read_b128 v[138:141], v127
	ds_read_b128 v[142:145], v127 offset:1024
	ds_read_b128 v[146:149], v127 offset:2048
	ds_read_b128 v[150:153], v127 offset:3072
	ds_read_b128 v[154:157], v127 offset:4096
	ds_read_b128 v[158:161], v127 offset:5120
	s_add_u32 m0, s12, 0x4000
	ds_read_b128 v[162:165], v121 offset:32768
	ds_read_b128 v[182:185], v121 offset:33792
	ds_read_b128 v[186:189], v108 offset:32768
	ds_read_b128 v[190:193], v108 offset:33792
	global_load_lds_dwordx4 v238, s[8:9]
	s_add_u32 m0, s12, 0x6000
	s_nop 0
	global_load_lds_dwordx4 v239, s[8:9]
	s_waitcnt lgkmcnt(4)
	s_barrier
	s_waitcnt lgkmcnt(0)
	s_setprio 1
	s_waitcnt lgkmcnt(0)
	v_mfma_f32_16x16x32_f16 v[94:97], v[162:165], v[138:141], v[94:97]
	v_mfma_f32_16x16x32_f16 v[90:93], v[162:165], v[146:149], v[90:93]
	v_mfma_f32_16x16x32_f16 v[86:89], v[162:165], v[154:157], v[86:89]
	v_mfma_f32_16x16x32_f16 v[82:85], v[186:189], v[138:141], v[82:85]
	v_mfma_f32_16x16x32_f16 v[78:81], v[186:189], v[146:149], v[78:81]
	v_mfma_f32_16x16x32_f16 v[66:69], v[186:189], v[154:157], v[66:69]
	v_mfma_f32_16x16x32_f16 v[94:97], v[182:185], v[142:145], v[94:97]
	v_mfma_f32_16x16x32_f16 v[90:93], v[182:185], v[150:153], v[90:93]
	v_mfma_f32_16x16x32_f16 v[86:89], v[182:185], v[158:161], v[86:89]
	v_mfma_f32_16x16x32_f16 v[82:85], v[190:193], v[142:145], v[82:85]
	v_mfma_f32_16x16x32_f16 v[78:81], v[190:193], v[150:153], v[78:81]
	v_mfma_f32_16x16x32_f16 v[66:69], v[190:193], v[158:161], v[66:69]
	s_setprio 0
	s_barrier
	s_add_u32 m0, s12, 0x18000
	ds_read_b128 v[194:197], v124
	ds_read_b128 v[198:201], v124 offset:1024
	ds_read_b128 v[202:205], v124 offset:2048
	ds_read_b128 v[206:209], v124 offset:3072
	ds_read_b128 v[210:213], v124 offset:4096
	ds_read_b128 v[214:217], v124 offset:5120
	global_load_lds_dwordx4 v242, s[10:11]
	s_add_u32 m0, s12, 0x1a000
	s_nop 0
	global_load_lds_dwordx4 v243, s[10:11]
	s_barrier
	s_waitcnt lgkmcnt(0)
	s_setprio 1
	s_waitcnt lgkmcnt(0)
	v_mfma_f32_16x16x32_f16 v[22:25], v[162:165], v[194:197], v[22:25]
	v_mfma_f32_16x16x32_f16 v[18:21], v[162:165], v[202:205], v[18:21]
	v_mfma_f32_16x16x32_f16 v[14:17], v[162:165], v[210:213], v[14:17]
	v_mfma_f32_16x16x32_f16 v[10:13], v[186:189], v[194:197], v[10:13]
	v_mfma_f32_16x16x32_f16 v[6:9], v[186:189], v[202:205], v[6:9]
	v_mfma_f32_16x16x32_f16 v[2:5], v[186:189], v[210:213], v[2:5]
	v_mfma_f32_16x16x32_f16 v[22:25], v[182:185], v[198:201], v[22:25]
	v_mfma_f32_16x16x32_f16 v[18:21], v[182:185], v[206:209], v[18:21]
	v_mfma_f32_16x16x32_f16 v[14:17], v[182:185], v[214:217], v[14:17]
	v_mfma_f32_16x16x32_f16 v[10:13], v[190:193], v[198:201], v[10:13]
	v_mfma_f32_16x16x32_f16 v[6:9], v[190:193], v[206:209], v[6:9]
	v_mfma_f32_16x16x32_f16 v[2:5], v[190:193], v[214:217], v[2:5]
	s_setprio 0
	s_add_u32 m0, s12, 0x8000
	s_barrier
	ds_read_b128 v[162:165], v121 offset:49152
	ds_read_b128 v[182:185], v121 offset:50176
	ds_read_b128 v[186:189], v108 offset:49152
	ds_read_b128 v[190:193], v108 offset:50176
	global_load_lds_dwordx4 v234, s[8:9]
	s_add_u32 m0, s12, 0xa000
	s_nop 0
	global_load_lds_dwordx4 v235, s[8:9]
	s_barrier
	s_waitcnt lgkmcnt(0)
	s_setprio 1
	s_waitcnt lgkmcnt(0)
	v_mfma_f32_16x16x32_f16 v[26:29], v[162:165], v[138:141], v[26:29]
	v_mfma_f32_16x16x32_f16 v[30:33], v[162:165], v[146:149], v[30:33]
	v_mfma_f32_16x16x32_f16 v[34:37], v[162:165], v[154:157], v[34:37]
	v_mfma_f32_16x16x32_f16 v[38:41], v[186:189], v[138:141], v[38:41]
	v_mfma_f32_16x16x32_f16 v[46:49], v[186:189], v[146:149], v[46:49]
	v_mfma_f32_16x16x32_f16 v[54:57], v[186:189], v[154:157], v[54:57]
	v_mfma_f32_16x16x32_f16 v[26:29], v[182:185], v[142:145], v[26:29]
	v_mfma_f32_16x16x32_f16 v[30:33], v[182:185], v[150:153], v[30:33]
	v_mfma_f32_16x16x32_f16 v[34:37], v[182:185], v[158:161], v[34:37]
	v_mfma_f32_16x16x32_f16 v[38:41], v[190:193], v[142:145], v[38:41]
	v_mfma_f32_16x16x32_f16 v[46:49], v[190:193], v[150:153], v[46:49]
	v_mfma_f32_16x16x32_f16 v[54:57], v[190:193], v[158:161], v[54:57]
	s_setprio 0
	s_barrier
	s_add_u32 m0, s12, 0x1c000
	s_nop 0
	global_load_lds_dwordx4 v246, s[10:11]
	s_add_u32 m0, s12, 0x1e000
	s_nop 0
	global_load_lds_dwordx4 v247, s[10:11]
	s_waitcnt vmcnt(6)
	s_barrier
	s_setprio 1
	v_mfma_f32_16x16x32_f16 v[42:45], v[162:165], v[194:197], v[42:45]
	v_mfma_f32_16x16x32_f16 v[50:53], v[162:165], v[202:205], v[50:53]
	v_mfma_f32_16x16x32_f16 v[58:61], v[162:165], v[210:213], v[58:61]
	v_mfma_f32_16x16x32_f16 v[62:65], v[186:189], v[194:197], v[62:65]
	v_mfma_f32_16x16x32_f16 v[70:73], v[186:189], v[202:205], v[70:73]
	v_mfma_f32_16x16x32_f16 v[74:77], v[186:189], v[210:213], v[74:77]
	v_mfma_f32_16x16x32_f16 v[42:45], v[182:185], v[198:201], v[42:45]
	v_mfma_f32_16x16x32_f16 v[50:53], v[182:185], v[206:209], v[50:53]
	v_mfma_f32_16x16x32_f16 v[58:61], v[182:185], v[214:217], v[58:61]
	v_mfma_f32_16x16x32_f16 v[62:65], v[190:193], v[198:201], v[62:65]
	v_mfma_f32_16x16x32_f16 v[70:73], v[190:193], v[206:209], v[70:73]
	v_mfma_f32_16x16x32_f16 v[74:77], v[190:193], v[214:217], v[74:77]
	s_setprio 0
	s_add_i32 s4, s4, 2
	s_add_u32 s2, s2, 0x100
	s_addc_u32 s3, s3, 0
	s_add_u32 s8, s8, 0x100
	s_addc_u32 s9, s9, 0
	s_add_u32 s10, s10, 0x100
	s_addc_u32 s11, s11, 0
	s_cmp_lt_u32 s4, 8
	s_barrier
	s_cbranch_scc1 .LBB1_52
	s_mov_b64 s[4:5], 0x580
	v_readfirstlane_b32 s2, v136
	v_lshl_add_u64 v[98:99], v[98:99], 0, s[4:5]
	s_mov_b32 m0, s2
	v_readfirstlane_b32 s2, v137
	ds_read_b128 v[102:105], v135
	ds_read_b128 v[110:113], v135 offset:1024
	ds_read_b128 v[114:117], v135 offset:2048
	ds_read_b128 v[128:131], v135 offset:3072
	ds_read_b128 v[138:141], v135 offset:4096
	ds_read_b128 v[142:145], v135 offset:5120
	ds_read_b128 v[146:149], v121
	ds_read_b128 v[150:153], v121 offset:1024
	ds_read_b128 v[154:157], v108
	ds_read_b128 v[158:161], v108 offset:1024
	global_load_lds_dwordx4 v[98:99], off
	v_lshl_add_u64 v[98:99], v[100:101], 0, s[4:5]
	s_mov_b32 m0, s2
	s_nop 0
	global_load_lds_dwordx4 v[98:99], off
	s_barrier
	s_waitcnt lgkmcnt(0)
	s_setprio 1
	s_waitcnt lgkmcnt(0)
	v_mfma_f32_16x16x32_f16 v[94:97], v[146:149], v[102:105], v[94:97]
	v_mfma_f32_16x16x32_f16 v[90:93], v[146:149], v[114:117], v[90:93]
	v_mfma_f32_16x16x32_f16 v[86:89], v[146:149], v[138:141], v[86:89]
	v_mfma_f32_16x16x32_f16 v[82:85], v[154:157], v[102:105], v[82:85]
	v_mfma_f32_16x16x32_f16 v[78:81], v[154:157], v[114:117], v[78:81]
	v_mfma_f32_16x16x32_f16 v[66:69], v[154:157], v[138:141], v[66:69]
	v_mfma_f32_16x16x32_f16 v[94:97], v[150:153], v[110:113], v[94:97]
	v_mfma_f32_16x16x32_f16 v[90:93], v[150:153], v[128:131], v[90:93]
	v_mfma_f32_16x16x32_f16 v[86:89], v[150:153], v[142:145], v[86:89]
	v_mfma_f32_16x16x32_f16 v[82:85], v[158:161], v[110:113], v[82:85]
	v_mfma_f32_16x16x32_f16 v[98:101], v[158:161], v[128:131], v[78:81]
	v_mfma_f32_16x16x32_f16 v[66:69], v[158:161], v[142:145], v[66:69]
	s_setprio 0
	s_barrier
	ds_read_b128 v[78:81], v134
	ds_read_b128 v[162:165], v134 offset:1024
	ds_read_b128 v[182:185], v134 offset:2048
	ds_read_b128 v[186:189], v134 offset:3072
	ds_read_b128 v[190:193], v134 offset:4096
	ds_read_b128 v[132:135], v134 offset:5120
	s_barrier
	s_waitcnt lgkmcnt(0)
	s_setprio 1
	s_waitcnt lgkmcnt(0)
	v_mfma_f32_16x16x32_f16 v[22:25], v[146:149], v[78:81], v[22:25]
	v_mfma_f32_16x16x32_f16 v[18:21], v[146:149], v[182:185], v[18:21]
	v_mfma_f32_16x16x32_f16 v[14:17], v[146:149], v[190:193], v[14:17]
	v_mfma_f32_16x16x32_f16 v[10:13], v[154:157], v[78:81], v[10:13]
	v_mfma_f32_16x16x32_f16 v[6:9], v[154:157], v[182:185], v[6:9]
	v_mfma_f32_16x16x32_f16 v[2:5], v[154:157], v[190:193], v[2:5]
	v_mfma_f32_16x16x32_f16 v[22:25], v[150:153], v[162:165], v[22:25]
	v_mfma_f32_16x16x32_f16 v[18:21], v[150:153], v[186:189], v[18:21]
	v_mfma_f32_16x16x32_f16 v[14:17], v[150:153], v[132:135], v[14:17]
	v_mfma_f32_16x16x32_f16 v[10:13], v[158:161], v[162:165], v[10:13]
	v_mfma_f32_16x16x32_f16 v[6:9], v[158:161], v[186:189], v[6:9]
	v_mfma_f32_16x16x32_f16 v[2:5], v[158:161], v[132:135], v[2:5]
	s_setprio 0
	s_barrier
	ds_read_b128 v[146:149], v121 offset:16384
	ds_read_b128 v[150:153], v121 offset:17408
	ds_read_b128 v[154:157], v108 offset:16384
	ds_read_b128 v[158:161], v108 offset:17408
	s_waitcnt vmcnt(4)
	s_barrier
	s_waitcnt lgkmcnt(0)
	s_setprio 1
	s_waitcnt lgkmcnt(0)
	v_mfma_f32_16x16x32_f16 v[26:29], v[146:149], v[102:105], v[26:29]
	v_mfma_f32_16x16x32_f16 v[30:33], v[146:149], v[114:117], v[30:33]
	v_mfma_f32_16x16x32_f16 v[34:37], v[146:149], v[138:141], v[34:37]
	v_mfma_f32_16x16x32_f16 v[38:41], v[154:157], v[102:105], v[38:41]
	v_mfma_f32_16x16x32_f16 v[46:49], v[154:157], v[114:117], v[46:49]
	v_mfma_f32_16x16x32_f16 v[26:29], v[150:153], v[110:113], v[26:29]
	v_mfma_f32_16x16x32_f16 v[30:33], v[150:153], v[128:131], v[30:33]
	v_mfma_f32_16x16x32_f16 v[34:37], v[150:153], v[142:145], v[34:37]
	v_mfma_f32_16x16x32_f16 v[38:41], v[158:161], v[110:113], v[38:41]
	v_mfma_f32_16x16x32_f16 v[46:49], v[158:161], v[128:131], v[46:49]
	v_mfma_f32_16x16x32_f16 v[54:57], v[154:157], v[138:141], v[54:57]
	v_mfma_f32_16x16x32_f16 v[54:57], v[158:161], v[142:145], v[54:57]
	s_setprio 0
	s_setprio 1
	v_mfma_f32_16x16x32_f16 v[58:61], v[146:149], v[190:193], v[58:61]
	v_mfma_f32_16x16x32_f16 v[110:113], v[150:153], v[132:135], v[58:61]
	v_mfma_f32_16x16x32_f16 v[58:61], v[154:157], v[78:81], v[62:65]
	v_mfma_f32_16x16x32_f16 v[42:45], v[146:149], v[78:81], v[42:45]
	v_mfma_f32_16x16x32_f16 v[114:117], v[158:161], v[162:165], v[58:61]
	v_mfma_f32_16x16x32_f16 v[58:61], v[154:157], v[182:185], v[70:73]
	v_mfma_f32_16x16x32_f16 v[42:45], v[150:153], v[162:165], v[42:45]
	v_mfma_f32_16x16x32_f16 v[50:53], v[146:149], v[182:185], v[50:53]
	v_mfma_f32_16x16x32_f16 v[128:131], v[158:161], v[186:189], v[58:61]
	v_mfma_f32_16x16x32_f16 v[58:61], v[154:157], v[190:193], v[74:77]
	v_mfma_f32_16x16x32_f16 v[50:53], v[150:153], v[186:189], v[50:53]
	v_mfma_f32_16x16x32_f16 v[132:135], v[158:161], v[132:135], v[58:61]
	s_setprio 0
	s_barrier
	ds_read_b128 v[136:139], v127
	ds_read_b128 v[140:143], v127 offset:1024
	ds_read_b128 v[144:147], v127 offset:2048
	ds_read_b128 v[148:151], v127 offset:3072
	ds_read_b128 v[152:155], v127 offset:4096
	ds_read_b128 v[156:159], v127 offset:5120
	ds_read_b128 v[74:77], v121 offset:32768
	ds_read_b128 v[160:163], v121 offset:33792
	ds_read_b128 v[164:167], v108 offset:32768
	ds_read_b128 v[182:185], v108 offset:33792
	s_waitcnt vmcnt(2)
	s_barrier
	s_waitcnt lgkmcnt(0)
	s_setprio 1
	s_waitcnt lgkmcnt(0)
	v_mfma_f32_16x16x32_f16 v[62:65], v[74:77], v[144:147], v[90:93]
	v_mfma_f32_16x16x32_f16 v[70:73], v[164:167], v[136:139], v[82:85]
	v_mfma_f32_16x16x32_f16 v[58:61], v[74:77], v[136:139], v[94:97]
	v_mfma_f32_16x16x32_f16 v[78:81], v[160:163], v[148:151], v[62:65]
	v_mfma_f32_16x16x32_f16 v[62:65], v[74:77], v[152:155], v[86:89]
	v_mfma_f32_16x16x32_f16 v[102:105], v[182:185], v[140:143], v[70:73]
	v_mfma_f32_16x16x32_f16 v[70:73], v[164:167], v[144:147], v[98:101]
	v_mfma_f32_16x16x32_f16 v[66:69], v[164:167], v[152:155], v[66:69]
	v_mfma_f32_16x16x32_f16 v[58:61], v[160:163], v[140:143], v[58:61]
	v_mfma_f32_16x16x32_f16 v[62:65], v[160:163], v[156:159], v[62:65]
	v_mfma_f32_16x16x32_f16 v[86:89], v[182:185], v[148:151], v[70:73]
	v_mfma_f32_16x16x32_f16 v[70:73], v[182:185], v[156:159], v[66:69]
	s_setprio 0
	s_barrier
	ds_read_b128 v[186:189], v124
	ds_read_b128 v[190:193], v124 offset:1024
	ds_read_b128 v[194:197], v124 offset:2048
	ds_read_b128 v[198:201], v124 offset:3072
	ds_read_b128 v[202:205], v124 offset:4096
	ds_read_b128 v[122:125], v124 offset:5120
	s_waitcnt vmcnt(0)
	s_barrier
	s_waitcnt lgkmcnt(0)
	s_setprio 1
	s_waitcnt lgkmcnt(0)
	v_mfma_f32_16x16x32_f16 v[22:25], v[74:77], v[186:189], v[22:25]
	v_mfma_f32_16x16x32_f16 v[18:21], v[74:77], v[194:197], v[18:21]
	v_mfma_f32_16x16x32_f16 v[14:17], v[74:77], v[202:205], v[14:17]
	v_mfma_f32_16x16x32_f16 v[10:13], v[164:167], v[186:189], v[10:13]
	v_mfma_f32_16x16x32_f16 v[6:9], v[164:167], v[194:197], v[6:9]
	v_mfma_f32_16x16x32_f16 v[2:5], v[164:167], v[202:205], v[2:5]
	v_mfma_f32_16x16x32_f16 v[94:97], v[160:163], v[190:193], v[22:25]
	v_mfma_f32_16x16x32_f16 v[82:85], v[160:163], v[198:201], v[18:21]
	v_mfma_f32_16x16x32_f16 v[66:69], v[160:163], v[122:125], v[14:17]
	v_mfma_f32_16x16x32_f16 v[98:101], v[182:185], v[190:193], v[10:13]
	v_mfma_f32_16x16x32_f16 v[90:93], v[182:185], v[198:201], v[6:9]
	v_mfma_f32_16x16x32_f16 v[74:77], v[182:185], v[122:125], v[2:5]
	s_setprio 0
	s_barrier
	ds_read_b128 v[10:13], v121 offset:49152
	ds_read_b128 v[160:163], v121 offset:50176
	ds_read_b128 v[164:167], v108 offset:49152
	ds_read_b128 v[182:185], v108 offset:50176
	s_barrier
	s_waitcnt lgkmcnt(0)
	s_setprio 1
	s_waitcnt lgkmcnt(0)
	v_mfma_f32_16x16x32_f16 v[2:5], v[10:13], v[136:139], v[26:29]
	v_mfma_f32_16x16x32_f16 v[18:21], v[164:167], v[136:139], v[38:41]
	v_mfma_f32_16x16x32_f16 v[14:17], v[160:163], v[140:143], v[2:5]
	v_mfma_f32_16x16x32_f16 v[2:5], v[10:13], v[144:147], v[30:33]
	v_mfma_f32_16x16x32_f16 v[38:41], v[182:185], v[140:143], v[18:21]
	v_mfma_f32_16x16x32_f16 v[18:21], v[164:167], v[144:147], v[46:49]
	v_mfma_f32_16x16x32_f16 v[6:9], v[160:163], v[148:151], v[2:5]
	v_mfma_f32_16x16x32_f16 v[2:5], v[10:13], v[152:155], v[34:37]
	v_mfma_f32_16x16x32_f16 v[26:29], v[182:185], v[148:151], v[18:21]
	v_mfma_f32_16x16x32_f16 v[18:21], v[164:167], v[152:155], v[54:57]
	v_mfma_f32_16x16x32_f16 v[2:5], v[160:163], v[156:159], v[2:5]
	v_mfma_f32_16x16x32_f16 v[18:21], v[182:185], v[156:159], v[18:21]
	s_setprio 0
	s_setprio 1
	v_mfma_f32_16x16x32_f16 v[34:37], v[164:167], v[186:189], v[114:117]
	v_mfma_f32_16x16x32_f16 v[22:25], v[10:13], v[186:189], v[42:45]
	v_mfma_f32_16x16x32_f16 v[46:49], v[182:185], v[190:193], v[34:37]
	v_mfma_f32_16x16x32_f16 v[34:37], v[164:167], v[194:197], v[128:131]
	v_mfma_f32_16x16x32_f16 v[30:33], v[160:163], v[190:193], v[22:25]
	v_mfma_f32_16x16x32_f16 v[22:25], v[10:13], v[194:197], v[50:53]
	v_mfma_f32_16x16x32_f16 v[10:13], v[10:13], v[202:205], v[110:113]
	v_mfma_f32_16x16x32_f16 v[42:45], v[182:185], v[198:201], v[34:37]
	v_mfma_f32_16x16x32_f16 v[34:37], v[164:167], v[202:205], v[132:135]
	v_mfma_f32_16x16x32_f16 v[22:25], v[160:163], v[198:201], v[22:25]
	v_mfma_f32_16x16x32_f16 v[10:13], v[160:163], v[122:125], v[10:13]
	v_mfma_f32_16x16x32_f16 v[34:37], v[182:185], v[122:125], v[34:37]
	s_setprio 0
	s_movk_i32 s2, 0x100
	v_cmp_gt_u32_e32 vcc, s2, v175
	s_barrier
	s_and_saveexec_b64 s[2:3], vcc
	s_cbranch_execz .LBB1_55
	s_barrier

.LBB1_65:
	s_or_b64 exec, exec, s[2:3]
	v_readlane_b32 s2, v230, 8
	v_mad_i64_i32 v[22:23], s[0:1], v17, s56, 0
	v_mad_i64_i32 v[18:19], s[0:1], v18, s56, 0
	v_mad_i64_i32 v[24:25], s[0:1], v120, s56, 0
	v_add_u32_e32 v137, s2, v16
	s_mov_b64 s[4:5], 0x80
	v_readfirstlane_b32 s0, v137
	v_add_u32_e32 v138, 0x2000, v137
	v_lshl_add_u64 v[6:7], v[6:7], 0, s[4:5]
	s_mov_b32 m0, s0
	v_readfirstlane_b32 s0, v138
	v_add_u32_e32 v139, 0x8000, v129
	v_mov_b32_e32 v46, 0
	v_mov_b32_e32 v47, 0
	v_mov_b32_e32 v48, 0
	v_mov_b32_e32 v49, 0
	v_mov_b32_e32 v74, 0
	v_mov_b32_e32 v75, 0
	v_mov_b32_e32 v76, 0
	v_mov_b32_e32 v77, 0
	v_mov_b32_e32 v86, 0
	v_mov_b32_e32 v87, 0
	v_mov_b32_e32 v88, 0
	v_mov_b32_e32 v89, 0
	v_mov_b32_e32 v90, 0
	v_mov_b32_e32 v91, 0
	v_mov_b32_e32 v92, 0
	v_mov_b32_e32 v93, 0
	v_mov_b32_e32 v94, 0
	v_mov_b32_e32 v95, 0
	v_mov_b32_e32 v96, 0
	v_mov_b32_e32 v97, 0
	v_mov_b32_e32 v26, 0
	v_mov_b32_e32 v27, 0
	v_mov_b32_e32 v28, 0
	v_mov_b32_e32 v29, 0
	v_mov_b32_e32 v34, 0
	v_mov_b32_e32 v35, 0
	v_mov_b32_e32 v36, 0
	v_mov_b32_e32 v37, 0
	v_mov_b32_e32 v50, 0
	v_mov_b32_e32 v51, 0
	v_mov_b32_e32 v52, 0
	v_mov_b32_e32 v53, 0
	v_mov_b32_e32 v30, 0
	v_mov_b32_e32 v31, 0
	v_mov_b32_e32 v32, 0
	v_mov_b32_e32 v33, 0
	v_mov_b32_e32 v38, 0
	v_mov_b32_e32 v39, 0
	v_mov_b32_e32 v40, 0
	v_mov_b32_e32 v41, 0
	v_mov_b32_e32 v54, 0
	v_mov_b32_e32 v55, 0
	v_mov_b32_e32 v56, 0
	v_mov_b32_e32 v57, 0
	v_mov_b32_e32 v62, 0
	v_mov_b32_e32 v63, 0
	v_mov_b32_e32 v64, 0
	v_mov_b32_e32 v65, 0
	v_mov_b32_e32 v42, 0
	v_mov_b32_e32 v43, 0
	v_mov_b32_e32 v44, 0
	v_mov_b32_e32 v45, 0
	v_mov_b32_e32 v58, 0
	v_mov_b32_e32 v59, 0
	v_mov_b32_e32 v60, 0
	v_mov_b32_e32 v61, 0
	v_mov_b32_e32 v66, 0
	v_mov_b32_e32 v67, 0
	v_mov_b32_e32 v68, 0
	v_mov_b32_e32 v69, 0
	v_mov_b32_e32 v70, 0
	v_mov_b32_e32 v71, 0
	v_mov_b32_e32 v72, 0
	v_mov_b32_e32 v73, 0
	v_mov_b32_e32 v78, 0
	v_mov_b32_e32 v79, 0
	v_mov_b32_e32 v80, 0
	v_mov_b32_e32 v81, 0
	v_mov_b32_e32 v82, 0
	v_mov_b32_e32 v83, 0
	v_mov_b32_e32 v84, 0
	v_mov_b32_e32 v85, 0
	s_waitcnt vmcnt(4)
	s_barrier
	global_load_lds_dwordx4 v[6:7], off
	v_lshl_add_u64 v[6:7], v[8:9], 0, s[4:5]
	s_mov_b32 m0, s0
	v_readfirstlane_b32 s0, v139
	v_add_u32_e32 v140, 0xa000, v129
	global_load_lds_dwordx4 v[6:7], off
	v_lshl_add_u64 v[6:7], v[10:11], 0, s[4:5]
	s_mov_b32 m0, s0
	v_readfirstlane_b32 s0, v140
	global_load_lds_dwordx4 v[6:7], off
	v_lshl_add_u64 v[6:7], v[12:13], 0, s[4:5]
	s_mov_b32 m0, s0
	s_mov_b64 s[0:1], 0x24080
	v_readlane_b32 s3, v230, 9
	global_load_lds_dwordx4 v[6:7], off
	v_lshl_add_u64 v[6:7], v[14:15], 0, s[0:1]
	v_add_u32_e32 v141, s3, v16
	v_lshl_add_u64 v[8:9], v[6:7], 0, v[22:23]
	v_readfirstlane_b32 s0, v141
	v_add_u32_e32 v142, 0x2000, v141
	v_lshl_add_u64 v[8:9], v[8:9], 0, v[2:3]
	s_mov_b32 m0, s0
	v_lshl_add_u64 v[6:7], v[6:7], 0, v[18:19]
	v_readfirstlane_b32 s0, v142
	global_load_lds_dwordx4 v[8:9], off
	v_lshl_add_u64 v[6:7], v[6:7], 0, v[4:5]
	s_mov_b32 m0, s0
	v_and_b32_e32 v125, 15, v107
	global_load_lds_dwordx4 v[6:7], off
	v_and_b32_e32 v6, 64, v107
	v_lshlrev_b32_e32 v123, 2, v107
	v_cmp_ne_u32_e64 s[0:1], 0, v6
	v_and_b32_e32 v124, 48, v107
	v_lshlrev_b32_e32 v6, 6, v125
	v_and_b32_e32 v7, 32, v123
	v_cndmask_b32_e64 v126, 0, 48, s[0:1]
	v_bitop3_b32 v6, v6, v7, v124 bitop3:0x36
	v_readlane_b32 s0, v230, 6
	v_ashrrev_i32_e32 v9, 2, v107
	v_and_b32_e32 v127, 0xffffffe0, v9
	v_add_u32_e32 v8, s0, v6
	v_readlane_b32 s0, v230, 7
	v_add_u32_e32 v10, s2, v6
	v_add_u32_e32 v11, s3, v6
	v_add_u32_e32 v9, s0, v6
	v_add_u32_e32 v13, 0, v6
	v_lshlrev_b32_e32 v6, 6, v107
	s_movk_i32 s0, 0x3c0
	v_mul_u32_u24_e32 v20, 0x600, v121
	v_mov_b32_e32 v21, v109
	v_and_or_b32 v6, v6, s0, v124
	v_lshl_add_u64 v[2:3], v[22:23], 0, v[2:3]
	v_xad_u32 v15, v6, v7, 0
	v_lshl_add_u64 v[6:7], v[2:3], 0, v[20:21]
	v_lshl_add_u64 v[4:5], v[18:19], 0, v[4:5]
	v_lshl_add_u64 v[104:105], s[40:41], 0, v[6:7]
	v_lshl_add_u64 v[6:7], v[4:5], 0, v[20:21]
	v_lshl_add_u64 v[110:111], s[40:41], 0, v[6:7]
	v_lshl_add_u64 v[6:7], v[2:3], 0, v[24:25]
	v_lshl_add_u64 v[2:3], v[2:3], 0, v[108:109]
	v_lshlrev_b32_e32 v14, 7, v127
	v_lshl_add_u64 v[116:117], s[40:41], 0, v[2:3]
	v_lshl_add_u64 v[2:3], v[4:5], 0, v[108:109]
	v_lshlrev_b32_e32 v12, 7, v126
	v_or_b32_e32 v16, 0x800, v14
	v_lshl_add_u64 v[112:113], s[38:39], 0, v[6:7]
	v_lshl_add_u64 v[6:7], v[4:5], 0, v[24:25]
	v_lshl_add_u64 v[118:119], s[40:41], 0, v[2:3]
	v_mov_b32_e32 v2, 0
	v_lshl_add_u64 v[114:115], s[38:39], 0, v[6:7]
	s_mov_b32 s2, -2
	s_mov_b64 s[0:1], 0
	v_add_u32_e32 v144, v8, v12
	v_add_u32_e32 v130, v13, v14
	v_add_u32_e32 v108, v15, v16
	v_add_u32_e32 v143, v9, v12
	v_add_u32_e32 v136, v10, v12
	v_add_u32_e32 v133, v11, v12
	v_mov_b32_e32 v3, v2
	v_mov_b32_e32 v4, v2
	v_mov_b32_e32 v5, v2
	v_mov_b32_e32 v6, v2
	v_mov_b32_e32 v7, v2
	v_mov_b32_e32 v8, v2
	v_mov_b32_e32 v9, v2
	v_mov_b32_e32 v10, v2
	v_mov_b32_e32 v11, v2
	v_mov_b32_e32 v12, v2
	v_mov_b32_e32 v13, v2
	v_mov_b32_e32 v18, v2
	v_mov_b32_e32 v19, v2
	v_mov_b32_e32 v20, v2
	v_mov_b32_e32 v21, v2
	v_mov_b32_e32 v14, v2
	v_mov_b32_e32 v15, v2
	v_mov_b32_e32 v16, v2
	v_mov_b32_e32 v17, v2
	v_mov_b32_e32 v22, v2
	v_mov_b32_e32 v23, v2
	v_mov_b32_e32 v24, v2
	v_mov_b32_e32 v25, v2
	s_waitcnt vmcnt(6)
	s_barrier
	v_add_u32_e32 v145, 0xc000, v129
	v_add_u32_e32 v146, 0xe000, v129
	v_readfirstlane_b32 s12, v129
	v_subrev_u32_e32 v248, s38, v112
	v_subrev_u32_e32 v249, s38, v114
	v_subrev_u32_e32 v250, s40, v104
	v_subrev_u32_e32 v251, s40, v110
	v_subrev_u32_e32 v246, s40, v116
	v_subrev_u32_e32 v247, s40, v118
	v_add_u32_e32 v232, 0x100, v248
	v_add_u32_e32 v233, 0x100, v249
	v_add_u32_e32 v234, 0x180, v248
	v_add_u32_e32 v235, 0x180, v249
	v_add_u32_e32 v236, 0x30080, v248
	v_add_u32_e32 v237, 0x30080, v249
	v_add_u32_e32 v238, 0x30100, v248
	v_add_u32_e32 v239, 0x30100, v249
	v_add_u32_e32 v240, 0x100, v250
	v_add_u32_e32 v241, 0x100, v251
	v_add_u32_e32 v242, 0x180, v250
	v_add_u32_e32 v243, 0x180, v251
	v_add_u32_e32 v244, 0x24100, v246
	v_add_u32_e32 v245, 0x24100, v247
	v_add_u32_e32 v246, 0x24180, v246
	v_add_u32_e32 v247, 0x24180, v247
	s_add_u32 s8, s38, s0
	s_addc_u32 s9, s39, s1
	s_add_u32 s10, s40, s0
	s_addc_u32 s11, s41, s1
.LBB1_66:
	ds_read_b128 v[148:151], v144
	ds_read_b128 v[152:155], v144 offset:1024
	ds_read_b128 v[156:159], v144 offset:2048
	ds_read_b128 v[160:163], v144 offset:3072
	ds_read_b128 v[164:167], v144 offset:4096
	ds_read_b128 v[174:177], v144 offset:5120
	s_add_u32 m0, s12, 0xc000
	ds_read_b128 v[178:181], v130
	ds_read_b128 v[182:185], v130 offset:1024
	ds_read_b128 v[186:189], v108
	ds_read_b128 v[190:193], v108 offset:1024
	global_load_lds_dwordx4 v236, s[8:9]
	s_add_u32 m0, s12, 0xe000
	s_nop 0
	global_load_lds_dwordx4 v237, s[8:9]
	s_waitcnt lgkmcnt(4)
	s_barrier
	s_waitcnt lgkmcnt(0)
	s_setprio 1
	s_waitcnt lgkmcnt(0)
	v_mfma_f32_16x16x32_f16 v[94:97], v[178:181], v[148:151], v[94:97]
	v_mfma_f32_16x16x32_f16 v[90:93], v[178:181], v[156:159], v[90:93]
	v_mfma_f32_16x16x32_f16 v[86:89], v[178:181], v[164:167], v[86:89]
	v_mfma_f32_16x16x32_f16 v[74:77], v[186:189], v[148:151], v[74:77]
	v_mfma_f32_16x16x32_f16 v[46:49], v[186:189], v[156:159], v[46:49]
	v_mfma_f32_16x16x32_f16 v[18:21], v[186:189], v[164:167], v[18:21]
	v_mfma_f32_16x16x32_f16 v[94:97], v[182:185], v[152:155], v[94:97]
	v_mfma_f32_16x16x32_f16 v[90:93], v[182:185], v[160:163], v[90:93]
	v_mfma_f32_16x16x32_f16 v[86:89], v[182:185], v[174:177], v[86:89]
	v_mfma_f32_16x16x32_f16 v[74:77], v[190:193], v[152:155], v[74:77]
	v_mfma_f32_16x16x32_f16 v[46:49], v[190:193], v[160:163], v[46:49]
	v_mfma_f32_16x16x32_f16 v[18:21], v[190:193], v[174:177], v[18:21]
	s_setprio 0
	s_barrier
	s_add_u32 m0, s12, 0x10000
	ds_read_b128 v[194:197], v143
	ds_read_b128 v[198:201], v143 offset:1024
	ds_read_b128 v[202:205], v143 offset:2048
	ds_read_b128 v[206:209], v143 offset:3072
	ds_read_b128 v[210:213], v143 offset:4096
	ds_read_b128 v[214:217], v143 offset:5120
	global_load_lds_dwordx4 v240, s[10:11]
	s_add_u32 m0, s12, 0x12000
	s_nop 0
	global_load_lds_dwordx4 v241, s[10:11]
	s_barrier
	s_waitcnt lgkmcnt(0)
	s_setprio 1
	s_waitcnt lgkmcnt(0)
	v_mfma_f32_16x16x32_f16 v[10:13], v[178:181], v[194:197], v[10:13]
	v_mfma_f32_16x16x32_f16 v[6:9], v[178:181], v[202:205], v[6:9]
	v_mfma_f32_16x16x32_f16 v[2:5], v[178:181], v[210:213], v[2:5]
	v_mfma_f32_16x16x32_f16 v[26:29], v[186:189], v[194:197], v[26:29]
	v_mfma_f32_16x16x32_f16 v[34:37], v[186:189], v[202:205], v[34:37]
	v_mfma_f32_16x16x32_f16 v[50:53], v[186:189], v[210:213], v[50:53]
	v_mfma_f32_16x16x32_f16 v[10:13], v[182:185], v[198:201], v[10:13]
	v_mfma_f32_16x16x32_f16 v[6:9], v[182:185], v[206:209], v[6:9]
	v_mfma_f32_16x16x32_f16 v[2:5], v[182:185], v[214:217], v[2:5]
	v_mfma_f32_16x16x32_f16 v[26:29], v[190:193], v[198:201], v[26:29]
	v_mfma_f32_16x16x32_f16 v[34:37], v[190:193], v[206:209], v[34:37]
	v_mfma_f32_16x16x32_f16 v[50:53], v[190:193], v[214:217], v[50:53]
	s_setprio 0
	s_add_u32 m0, s12, 0x0
	s_barrier
	ds_read_b128 v[178:181], v130 offset:16384
	ds_read_b128 v[182:185], v130 offset:17408
	ds_read_b128 v[186:189], v108 offset:16384
	ds_read_b128 v[190:193], v108 offset:17408
	global_load_lds_dwordx4 v232, s[8:9]
	s_add_u32 m0, s12, 0x2000
	s_nop 0
	global_load_lds_dwordx4 v233, s[8:9]
	s_barrier
	s_waitcnt lgkmcnt(0)
	s_setprio 1
	s_waitcnt lgkmcnt(0)
	v_mfma_f32_16x16x32_f16 v[14:17], v[178:181], v[148:151], v[14:17]
	v_mfma_f32_16x16x32_f16 v[22:25], v[178:181], v[156:159], v[22:25]
	v_mfma_f32_16x16x32_f16 v[30:33], v[178:181], v[164:167], v[30:33]
	v_mfma_f32_16x16x32_f16 v[38:41], v[186:189], v[148:151], v[38:41]
	v_mfma_f32_16x16x32_f16 v[54:57], v[186:189], v[156:159], v[54:57]
	v_mfma_f32_16x16x32_f16 v[62:65], v[186:189], v[164:167], v[62:65]
	v_mfma_f32_16x16x32_f16 v[14:17], v[182:185], v[152:155], v[14:17]
	v_mfma_f32_16x16x32_f16 v[22:25], v[182:185], v[160:163], v[22:25]
	v_mfma_f32_16x16x32_f16 v[30:33], v[182:185], v[174:177], v[30:33]
	v_mfma_f32_16x16x32_f16 v[38:41], v[190:193], v[152:155], v[38:41]
	v_mfma_f32_16x16x32_f16 v[54:57], v[190:193], v[160:163], v[54:57]
	v_mfma_f32_16x16x32_f16 v[62:65], v[190:193], v[174:177], v[62:65]
	s_setprio 0
	s_barrier
	s_add_u32 m0, s12, 0x14000
	s_nop 0
	global_load_lds_dwordx4 v244, s[10:11]
	s_add_u32 m0, s12, 0x16000
	s_nop 0
	global_load_lds_dwordx4 v245, s[10:11]
	s_waitcnt vmcnt(6)
	s_barrier
	s_setprio 1
	v_mfma_f32_16x16x32_f16 v[42:45], v[178:181], v[194:197], v[42:45]
	v_mfma_f32_16x16x32_f16 v[58:61], v[178:181], v[202:205], v[58:61]
	v_mfma_f32_16x16x32_f16 v[66:69], v[178:181], v[210:213], v[66:69]
	v_mfma_f32_16x16x32_f16 v[70:73], v[186:189], v[194:197], v[70:73]
	v_mfma_f32_16x16x32_f16 v[78:81], v[186:189], v[202:205], v[78:81]
	v_mfma_f32_16x16x32_f16 v[82:85], v[186:189], v[210:213], v[82:85]
	v_mfma_f32_16x16x32_f16 v[42:45], v[182:185], v[198:201], v[42:45]
	v_mfma_f32_16x16x32_f16 v[58:61], v[182:185], v[206:209], v[58:61]
	v_mfma_f32_16x16x32_f16 v[66:69], v[182:185], v[214:217], v[66:69]
	v_mfma_f32_16x16x32_f16 v[70:73], v[190:193], v[198:201], v[70:73]
	v_mfma_f32_16x16x32_f16 v[78:81], v[190:193], v[206:209], v[78:81]
	v_mfma_f32_16x16x32_f16 v[82:85], v[190:193], v[214:217], v[82:85]
	s_setprio 0
	s_barrier
	ds_read_b128 v[148:151], v136
	ds_read_b128 v[152:155], v136 offset:1024
	ds_read_b128 v[156:159], v136 offset:2048
	ds_read_b128 v[160:163], v136 offset:3072
	ds_read_b128 v[164:167], v136 offset:4096
	ds_read_b128 v[174:177], v136 offset:5120
	s_add_u32 m0, s12, 0x4000
	ds_read_b128 v[178:181], v130 offset:32768
	ds_read_b128 v[182:185], v130 offset:33792
	ds_read_b128 v[186:189], v108 offset:32768
	ds_read_b128 v[190:193], v108 offset:33792
	global_load_lds_dwordx4 v238, s[8:9]
	s_add_u32 m0, s12, 0x6000
	s_nop 0
	global_load_lds_dwordx4 v239, s[8:9]
	s_waitcnt lgkmcnt(4)
	s_barrier
	s_waitcnt lgkmcnt(0)
	s_setprio 1
	s_waitcnt lgkmcnt(0)
	v_mfma_f32_16x16x32_f16 v[94:97], v[178:181], v[148:151], v[94:97]
	v_mfma_f32_16x16x32_f16 v[90:93], v[178:181], v[156:159], v[90:93]
	v_mfma_f32_16x16x32_f16 v[86:89], v[178:181], v[164:167], v[86:89]
	v_mfma_f32_16x16x32_f16 v[74:77], v[186:189], v[148:151], v[74:77]
	v_mfma_f32_16x16x32_f16 v[46:49], v[186:189], v[156:159], v[46:49]
	v_mfma_f32_16x16x32_f16 v[18:21], v[186:189], v[164:167], v[18:21]
	v_mfma_f32_16x16x32_f16 v[94:97], v[182:185], v[152:155], v[94:97]
	v_mfma_f32_16x16x32_f16 v[90:93], v[182:185], v[160:163], v[90:93]
	v_mfma_f32_16x16x32_f16 v[86:89], v[182:185], v[174:177], v[86:89]
	v_mfma_f32_16x16x32_f16 v[74:77], v[190:193], v[152:155], v[74:77]
	v_mfma_f32_16x16x32_f16 v[46:49], v[190:193], v[160:163], v[46:49]
	v_mfma_f32_16x16x32_f16 v[18:21], v[190:193], v[174:177], v[18:21]
	s_setprio 0
	s_barrier
	s_add_u32 m0, s12, 0x18000
	ds_read_b128 v[194:197], v133
	ds_read_b128 v[198:201], v133 offset:1024
	ds_read_b128 v[202:205], v133 offset:2048
	ds_read_b128 v[206:209], v133 offset:3072
	ds_read_b128 v[210:213], v133 offset:4096
	ds_read_b128 v[214:217], v133 offset:5120
	global_load_lds_dwordx4 v242, s[10:11]
	s_add_u32 m0, s12, 0x1a000
	s_nop 0
	global_load_lds_dwordx4 v243, s[10:11]
	s_barrier
	s_waitcnt lgkmcnt(0)
	s_setprio 1
	s_waitcnt lgkmcnt(0)
	v_mfma_f32_16x16x32_f16 v[10:13], v[178:181], v[194:197], v[10:13]
	v_mfma_f32_16x16x32_f16 v[6:9], v[178:181], v[202:205], v[6:9]
	v_mfma_f32_16x16x32_f16 v[2:5], v[178:181], v[210:213], v[2:5]
	v_mfma_f32_16x16x32_f16 v[26:29], v[186:189], v[194:197], v[26:29]
	v_mfma_f32_16x16x32_f16 v[34:37], v[186:189], v[202:205], v[34:37]
	v_mfma_f32_16x16x32_f16 v[50:53], v[186:189], v[210:213], v[50:53]
	v_mfma_f32_16x16x32_f16 v[10:13], v[182:185], v[198:201], v[10:13]
	v_mfma_f32_16x16x32_f16 v[6:9], v[182:185], v[206:209], v[6:9]
	v_mfma_f32_16x16x32_f16 v[2:5], v[182:185], v[214:217], v[2:5]
	v_mfma_f32_16x16x32_f16 v[26:29], v[190:193], v[198:201], v[26:29]
	v_mfma_f32_16x16x32_f16 v[34:37], v[190:193], v[206:209], v[34:37]
	v_mfma_f32_16x16x32_f16 v[50:53], v[190:193], v[214:217], v[50:53]
	s_setprio 0
	s_add_u32 m0, s12, 0x8000
	s_barrier
	ds_read_b128 v[178:181], v130 offset:49152
	ds_read_b128 v[182:185], v130 offset:50176
	ds_read_b128 v[186:189], v108 offset:49152
	ds_read_b128 v[190:193], v108 offset:50176
	global_load_lds_dwordx4 v234, s[8:9]
	s_add_u32 m0, s12, 0xa000
	s_nop 0
	global_load_lds_dwordx4 v235, s[8:9]
	s_barrier
	s_waitcnt lgkmcnt(0)
	s_setprio 1
	s_waitcnt lgkmcnt(0)
	v_mfma_f32_16x16x32_f16 v[14:17], v[178:181], v[148:151], v[14:17]
	v_mfma_f32_16x16x32_f16 v[22:25], v[178:181], v[156:159], v[22:25]
	v_mfma_f32_16x16x32_f16 v[30:33], v[178:181], v[164:167], v[30:33]
	v_mfma_f32_16x16x32_f16 v[38:41], v[186:189], v[148:151], v[38:41]
	v_mfma_f32_16x16x32_f16 v[54:57], v[186:189], v[156:159], v[54:57]
	v_mfma_f32_16x16x32_f16 v[62:65], v[186:189], v[164:167], v[62:65]
	v_mfma_f32_16x16x32_f16 v[14:17], v[182:185], v[152:155], v[14:17]
	v_mfma_f32_16x16x32_f16 v[22:25], v[182:185], v[160:163], v[22:25]
	v_mfma_f32_16x16x32_f16 v[30:33], v[182:185], v[174:177], v[30:33]
	v_mfma_f32_16x16x32_f16 v[38:41], v[190:193], v[152:155], v[38:41]
	v_mfma_f32_16x16x32_f16 v[54:57], v[190:193], v[160:163], v[54:57]
	v_mfma_f32_16x16x32_f16 v[62:65], v[190:193], v[174:177], v[62:65]
	s_setprio 0
	s_barrier
	s_add_u32 m0, s12, 0x1c000
	s_nop 0
	global_load_lds_dwordx4 v246, s[10:11]
	s_add_u32 m0, s12, 0x1e000
	s_nop 0
	global_load_lds_dwordx4 v247, s[10:11]
	s_waitcnt vmcnt(6)
	s_barrier
	s_setprio 1
	v_mfma_f32_16x16x32_f16 v[42:45], v[178:181], v[194:197], v[42:45]
	v_mfma_f32_16x16x32_f16 v[58:61], v[178:181], v[202:205], v[58:61]
	v_mfma_f32_16x16x32_f16 v[66:69], v[178:181], v[210:213], v[66:69]
	v_mfma_f32_16x16x32_f16 v[70:73], v[186:189], v[194:197], v[70:73]
	v_mfma_f32_16x16x32_f16 v[78:81], v[186:189], v[202:205], v[78:81]
	v_mfma_f32_16x16x32_f16 v[82:85], v[186:189], v[210:213], v[82:85]
	v_mfma_f32_16x16x32_f16 v[42:45], v[182:185], v[198:201], v[42:45]
	v_mfma_f32_16x16x32_f16 v[58:61], v[182:185], v[206:209], v[58:61]
	v_mfma_f32_16x16x32_f16 v[66:69], v[182:185], v[214:217], v[66:69]
	v_mfma_f32_16x16x32_f16 v[70:73], v[190:193], v[198:201], v[70:73]
	v_mfma_f32_16x16x32_f16 v[78:81], v[190:193], v[206:209], v[78:81]
	v_mfma_f32_16x16x32_f16 v[82:85], v[190:193], v[214:217], v[82:85]
	s_setprio 0
	s_add_i32 s2, s2, 2
	s_add_u32 s0, s0, 0x100
	s_addc_u32 s1, s1, 0
	s_add_u32 s8, s8, 0x100
	s_addc_u32 s9, s9, 0
	s_add_u32 s10, s10, 0x100
	s_addc_u32 s11, s11, 0
	s_cmp_lt_u32 s2, 8
	s_barrier
	s_cbranch_scc1 .LBB1_66
	v_readlane_b32 s10, v230, 2
	v_readlane_b32 s11, v230, 3
	v_or_b32_e32 v238, v126, v125
	v_add_u32_e32 v238, v238, v121
	v_lshlrev_b32_e32 v232, 1, v238
	v_and_b32_e32 v232, -4, v232
	v_add_u32_e32 v233, 16, v238
	v_lshlrev_b32_e32 v233, 1, v233
	v_and_b32_e32 v233, -4, v233
	v_add_u32_e32 v234, 32, v238
	v_lshlrev_b32_e32 v234, 1, v234
	v_and_b32_e32 v234, -4, v234
	v_add_u32_e32 v235, 0x60, v238
	v_lshlrev_b32_e32 v235, 1, v235
	v_and_b32_e32 v235, -4, v235
	v_add_u32_e32 v236, 0x70, v238
	v_lshlrev_b32_e32 v236, 1, v236
	v_and_b32_e32 v236, -4, v236
	v_add_u32_e32 v237, 0x80, v238
	v_lshlrev_b32_e32 v237, 1, v237
	v_and_b32_e32 v237, -4, v237
	global_load_dword v232, v232, s[48:49]
	global_load_dword v233, v233, s[48:49]
	global_load_dword v234, v234, s[48:49]
	global_load_dword v235, v235, s[48:49]
	global_load_dword v236, v236, s[48:49]
	global_load_dword v237, v237, s[48:49]
	s_mov_b32 s32, 0x2aaaaaab
	v_mul_hi_u32 v239, v107, s32
	v_lshrrev_b32_e32 v239, 4, v239
	v_mul_u32_u24_e32 v239, 0x60, v239
	v_sub_u32_e32 v239, v107, v239
	v_lshrrev_b32_e32 v240, 1, v121
	v_add_u32_e32 v239, v239, v240
	v_lshlrev_b32_e32 v239, 3, v239
	global_load_dwordx2 v[240:241], v239, s[10:11]
	global_load_dwordx2 v[242:243], v239, s[10:11] offset:3072
	s_mov_b64 s[2:3], 0x580
	v_readfirstlane_b32 s0, v145
	v_lshl_add_u64 v[100:101], v[100:101], 0, s[2:3]
	s_mov_b32 m0, s0
	v_readfirstlane_b32 s0, v146
	ds_read_b128 v[110:113], v144
	ds_read_b128 v[114:117], v144 offset:1024
	ds_read_b128 v[138:141], v144 offset:2048
	ds_read_b128 v[148:151], v144 offset:3072
	ds_read_b128 v[152:155], v144 offset:4096
	ds_read_b128 v[156:159], v144 offset:5120
	ds_read_b128 v[160:163], v130
	ds_read_b128 v[164:167], v130 offset:1024
	ds_read_b128 v[174:177], v108
	ds_read_b128 v[178:181], v108 offset:1024
	global_load_lds_dwordx4 v[100:101], off
	v_lshl_add_u64 v[100:101], v[102:103], 0, s[2:3]
	s_mov_b32 m0, s0
	s_nop 0
	global_load_lds_dwordx4 v[100:101], off
	s_barrier
	s_waitcnt lgkmcnt(0)
	s_setprio 1
	s_waitcnt lgkmcnt(0)
	v_mfma_f32_16x16x32_f16 v[94:97], v[160:163], v[110:113], v[94:97]
	v_mfma_f32_16x16x32_f16 v[90:93], v[160:163], v[138:141], v[90:93]
	v_mfma_f32_16x16x32_f16 v[86:89], v[160:163], v[152:155], v[86:89]
	v_mfma_f32_16x16x32_f16 v[74:77], v[174:177], v[110:113], v[74:77]
	v_mfma_f32_16x16x32_f16 v[18:21], v[174:177], v[152:155], v[18:21]
	v_mfma_f32_16x16x32_f16 v[94:97], v[164:167], v[114:117], v[94:97]
	v_mfma_f32_16x16x32_f16 v[90:93], v[164:167], v[148:151], v[90:93]
	v_mfma_f32_16x16x32_f16 v[86:89], v[164:167], v[156:159], v[86:89]
	v_mfma_f32_16x16x32_f16 v[74:77], v[178:181], v[114:117], v[74:77]
	v_mfma_f32_16x16x32_f16 v[46:49], v[174:177], v[138:141], v[46:49]
	v_mfma_f32_16x16x32_f16 v[18:21], v[178:181], v[156:159], v[18:21]
	v_mfma_f32_16x16x32_f16 v[100:103], v[178:181], v[148:151], v[46:49]
	s_setprio 0
	s_barrier
	s_nop 3
	ds_read_b128 v[46:49], v143
	ds_read_b128 v[144:147], v143 offset:1024
	ds_read_b128 v[182:185], v143 offset:2048
	ds_read_b128 v[186:189], v143 offset:3072
	ds_read_b128 v[190:193], v143 offset:4096
	ds_read_b128 v[194:197], v143 offset:5120
	s_barrier
	s_waitcnt lgkmcnt(0)
	s_setprio 1
	s_waitcnt lgkmcnt(0)
	v_mfma_f32_16x16x32_f16 v[34:37], v[174:177], v[182:185], v[34:37]
	v_mfma_f32_16x16x32_f16 v[10:13], v[160:163], v[46:49], v[10:13]
	v_mfma_f32_16x16x32_f16 v[6:9], v[160:163], v[182:185], v[6:9]
	v_mfma_f32_16x16x32_f16 v[2:5], v[160:163], v[190:193], v[2:5]
	v_mfma_f32_16x16x32_f16 v[26:29], v[174:177], v[46:49], v[26:29]
	v_mfma_f32_16x16x32_f16 v[160:163], v[178:181], v[186:189], v[34:37]
	v_mfma_f32_16x16x32_f16 v[34:37], v[174:177], v[190:193], v[50:53]
	v_mfma_f32_16x16x32_f16 v[10:13], v[164:167], v[144:147], v[10:13]
	v_mfma_f32_16x16x32_f16 v[6:9], v[164:167], v[186:189], v[6:9]
	v_mfma_f32_16x16x32_f16 v[2:5], v[164:167], v[194:197], v[2:5]
	v_mfma_f32_16x16x32_f16 v[26:29], v[178:181], v[144:147], v[26:29]
	v_mfma_f32_16x16x32_f16 v[50:53], v[178:181], v[194:197], v[34:37]
	s_setprio 0
	s_barrier
	s_nop 0
	ds_read_b128 v[34:37], v130 offset:16384
	ds_read_b128 v[164:167], v130 offset:17408
	ds_read_b128 v[174:177], v108 offset:16384
	ds_read_b128 v[178:181], v108 offset:17408
	s_waitcnt vmcnt(12)
	s_barrier
	s_waitcnt lgkmcnt(0)
	s_setprio 1
	s_waitcnt lgkmcnt(0)
	v_mfma_f32_16x16x32_f16 v[22:25], v[34:37], v[138:141], v[22:25]
	v_mfma_f32_16x16x32_f16 v[198:201], v[164:167], v[148:151], v[22:25]
	v_mfma_f32_16x16x32_f16 v[22:25], v[34:37], v[152:155], v[30:33]
	v_mfma_f32_16x16x32_f16 v[30:33], v[164:167], v[156:159], v[22:25]
	v_mfma_f32_16x16x32_f16 v[22:25], v[174:177], v[110:113], v[38:41]
	v_mfma_f32_16x16x32_f16 v[14:17], v[34:37], v[110:113], v[14:17]
	v_mfma_f32_16x16x32_f16 v[110:113], v[178:181], v[114:117], v[22:25]
	v_mfma_f32_16x16x32_f16 v[22:25], v[174:177], v[138:141], v[54:57]
	v_mfma_f32_16x16x32_f16 v[14:17], v[164:167], v[114:117], v[14:17]
	v_mfma_f32_16x16x32_f16 v[54:57], v[178:181], v[148:151], v[22:25]
	v_mfma_f32_16x16x32_f16 v[22:25], v[174:177], v[152:155], v[62:65]
	v_mfma_f32_16x16x32_f16 v[114:117], v[178:181], v[156:159], v[22:25]
	s_setprio 0
	s_setprio 1
	v_mfma_f32_16x16x32_f16 v[22:25], v[34:37], v[46:49], v[42:45]
	v_mfma_f32_16x16x32_f16 v[138:141], v[164:167], v[144:147], v[22:25]
	v_mfma_f32_16x16x32_f16 v[22:25], v[34:37], v[182:185], v[58:61]
	v_mfma_f32_16x16x32_f16 v[148:151], v[164:167], v[186:189], v[22:25]
	v_mfma_f32_16x16x32_f16 v[22:25], v[34:37], v[190:193], v[66:69]
	v_mfma_f32_16x16x32_f16 v[152:155], v[164:167], v[194:197], v[22:25]
	v_mfma_f32_16x16x32_f16 v[22:25], v[174:177], v[46:49], v[70:73]
	v_mfma_f32_16x16x32_f16 v[142:145], v[178:181], v[144:147], v[22:25]
	v_mfma_f32_16x16x32_f16 v[22:25], v[174:177], v[182:185], v[78:81]
	v_mfma_f32_16x16x32_f16 v[156:159], v[178:181], v[186:189], v[22:25]
	v_mfma_f32_16x16x32_f16 v[22:25], v[174:177], v[190:193], v[82:85]
	v_mfma_f32_16x16x32_f16 v[164:167], v[178:181], v[194:197], v[22:25]
	s_setprio 0
	s_barrier
	ds_read_b128 v[58:61], v136
	ds_read_b128 v[174:177], v136 offset:1024
	ds_read_b128 v[178:181], v136 offset:2048
	ds_read_b128 v[182:185], v136 offset:3072
	ds_read_b128 v[186:189], v136 offset:4096
	ds_read_b128 v[134:137], v136 offset:5120
	ds_read_b128 v[34:37], v130 offset:32768
	ds_read_b128 v[62:65], v130 offset:33792
	ds_read_b128 v[78:81], v108 offset:32768
	ds_read_b128 v[190:193], v108 offset:33792
	s_waitcnt vmcnt(2)
	s_barrier
	s_waitcnt lgkmcnt(0)
	s_setprio 1
	s_waitcnt lgkmcnt(0)
	v_mfma_f32_16x16x32_f16 v[22:25], v[34:37], v[58:61], v[94:97]
	v_mfma_f32_16x16x32_f16 v[82:85], v[62:65], v[174:177], v[22:25]
	v_mfma_f32_16x16x32_f16 v[22:25], v[34:37], v[178:181], v[90:93]
	v_mfma_f32_16x16x32_f16 v[70:73], v[62:65], v[182:185], v[22:25]
	v_mfma_f32_16x16x32_f16 v[22:25], v[34:37], v[186:189], v[86:89]
	v_mfma_f32_16x16x32_f16 v[46:49], v[62:65], v[134:137], v[22:25]
	v_mfma_f32_16x16x32_f16 v[22:25], v[78:81], v[58:61], v[74:77]
	v_mfma_f32_16x16x32_f16 v[86:89], v[190:193], v[174:177], v[22:25]
	v_mfma_f32_16x16x32_f16 v[22:25], v[78:81], v[178:181], v[100:103]
	v_mfma_f32_16x16x32_f16 v[18:21], v[78:81], v[186:189], v[18:21]
	v_mfma_f32_16x16x32_f16 v[66:69], v[190:193], v[182:185], v[22:25]
	v_mfma_f32_16x16x32_f16 v[42:45], v[190:193], v[134:137], v[18:21]
	s_setprio 0
	s_barrier
	ds_read_b128 v[100:103], v133
	ds_read_b128 v[194:197], v133 offset:1024
	ds_read_b128 v[202:205], v133 offset:2048
	ds_read_b128 v[206:209], v133 offset:3072
	ds_read_b128 v[210:213], v133 offset:4096
	ds_read_b128 v[214:217], v133 offset:5120
	s_waitcnt vmcnt(0)
	s_barrier
	s_waitcnt lgkmcnt(0)
	s_setprio 1
	s_waitcnt lgkmcnt(0)
	v_mfma_f32_16x16x32_f16 v[6:9], v[34:37], v[202:205], v[6:9]
	v_mfma_f32_16x16x32_f16 v[2:5], v[34:37], v[210:213], v[2:5]
	v_mfma_f32_16x16x32_f16 v[22:25], v[62:65], v[206:209], v[6:9]
	v_mfma_f32_16x16x32_f16 v[6:9], v[62:65], v[214:217], v[2:5]
	v_mfma_f32_16x16x32_f16 v[2:5], v[78:81], v[100:103], v[26:29]
	v_mfma_f32_16x16x32_f16 v[10:13], v[34:37], v[100:103], v[10:13]
	v_mfma_f32_16x16x32_f16 v[34:37], v[190:193], v[194:197], v[2:5]
	v_mfma_f32_16x16x32_f16 v[2:5], v[78:81], v[202:205], v[160:163]
	v_mfma_f32_16x16x32_f16 v[18:21], v[190:193], v[206:209], v[2:5]
	v_mfma_f32_16x16x32_f16 v[2:5], v[78:81], v[210:213], v[50:53]
	v_mfma_f32_16x16x32_f16 v[38:41], v[62:65], v[194:197], v[10:13]
	v_mfma_f32_16x16x32_f16 v[2:5], v[190:193], v[214:217], v[2:5]
	s_setprio 0
	s_barrier
	ds_read_b128 v[10:13], v130 offset:49152
	ds_read_b128 v[26:29], v130 offset:50176
	ds_read_b128 v[128:131], v108 offset:49152
	ds_read_b128 v[160:163], v108 offset:50176
	s_barrier
	s_waitcnt lgkmcnt(0)
	s_setprio 1
	s_waitcnt lgkmcnt(0)
	v_mfma_f32_16x16x32_f16 v[14:17], v[10:13], v[58:61], v[14:17]
	v_mfma_f32_16x16x32_f16 v[90:93], v[26:29], v[174:177], v[14:17]
	v_mfma_f32_16x16x32_f16 v[14:17], v[10:13], v[178:181], v[198:201]
	v_mfma_f32_16x16x32_f16 v[78:81], v[26:29], v[182:185], v[14:17]
	v_mfma_f32_16x16x32_f16 v[14:17], v[10:13], v[186:189], v[30:33]
	v_mfma_f32_16x16x32_f16 v[62:65], v[26:29], v[134:137], v[14:17]
	v_mfma_f32_16x16x32_f16 v[14:17], v[128:131], v[58:61], v[110:113]
	v_mfma_f32_16x16x32_f16 v[94:97], v[160:163], v[174:177], v[14:17]
	v_mfma_f32_16x16x32_f16 v[14:17], v[128:131], v[178:181], v[54:57]
	v_mfma_f32_16x16x32_f16 v[74:77], v[160:163], v[182:185], v[14:17]
	v_mfma_f32_16x16x32_f16 v[14:17], v[128:131], v[186:189], v[114:117]
	v_mfma_f32_16x16x32_f16 v[58:61], v[160:163], v[134:137], v[14:17]
	s_setprio 0
	s_setprio 1
	v_mfma_f32_16x16x32_f16 v[14:17], v[10:13], v[100:103], v[138:141]
	v_mfma_f32_16x16x32_f16 v[54:57], v[26:29], v[194:197], v[14:17]
	v_mfma_f32_16x16x32_f16 v[14:17], v[10:13], v[202:205], v[148:151]
	v_mfma_f32_16x16x32_f16 v[10:13], v[10:13], v[210:213], v[152:155]
	v_mfma_f32_16x16x32_f16 v[30:33], v[26:29], v[206:209], v[14:17]
	v_mfma_f32_16x16x32_f16 v[14:17], v[26:29], v[214:217], v[10:13]
	v_mfma_f32_16x16x32_f16 v[10:13], v[128:131], v[100:103], v[142:145]
	v_mfma_f32_16x16x32_f16 v[50:53], v[160:163], v[194:197], v[10:13]
	v_mfma_f32_16x16x32_f16 v[10:13], v[128:131], v[202:205], v[156:159]
	v_mfma_f32_16x16x32_f16 v[26:29], v[160:163], v[206:209], v[10:13]
	v_mfma_f32_16x16x32_f16 v[10:13], v[128:131], v[210:213], v[164:167]
	v_mfma_f32_16x16x32_f16 v[10:13], v[160:163], v[214:217], v[10:13]
	s_setprio 0
	s_movk_i32 s0, 0x100
	v_cmp_gt_u32_e64 s[0:1], s0, v107
	s_barrier
	s_and_saveexec_b64 s[2:3], s[0:1]
	s_cbranch_execz .LBB1_69
	s_barrier
